# final6 with the chunk-major exp/PV section rescheduled: row-sum adds of each key chunk moved into that chunk's own MFMA gaps, bf16 converts trail the exps by one gap, V set B moved to free VGPRs v186-
# baseline (speedup 1.0000x reference)
; #define LAS __attribute__((address_space(3)))
; DI float max_x32(float v, int lane) { return fmaxf(v, bpx(v, lane, 32)); }
; #define MFMA32(a, b, c) __builtin_amdgcn_mfma_f32_32x32x16_bf16((a), (b), (c), 0, 0, 0)
; DI unsigned at_cvtpk(float lo, float hi) { unsigned r; asm volatile("v_cvt_pk_bf16_f32 %0, %1, %2" : "=v"(r) : "v"(lo), "v"(hi)); return r; }
; DI float at_softmax(f32x16& p0, f32x16& p1, float& m_run, bool first, bool nearb, LAS const float* tabp, int lane) {
;     if (nearb) {
; #pragma unroll
;         for (int i = 0; i < 16; ++i) { p0[i] += tabp[8 * (i >> 2) + (i & 3)]; p1[i] += tabp[32 + 8 * (i >> 2) + (i & 3)]; }
;     }
;     float mx = p0[0];
; #pragma unroll
;     for (int i = 1; i < 16; ++i) mx = fmaxf(mx, p0[i]);
; #pragma unroll
;     for (int i = 0; i < 16; ++i) mx = fmaxf(mx, p1[i]);
;     float alpha = 1.f;
;     if (first || !__all(mx <= AT_THR)) {
;         mx = max_x32(mx, lane);
;         const float dl = first ? mx : fmaxf(mx, 0.f);
;         alpha = first ? 1.f : __builtin_amdgcn_exp2f(-dl); m_run += dl;
; #pragma unroll
;         for (int i = 0; i < 16; ++i) { p0[i] -= dl; p1[i] -= dl; }
;     }
; #pragma unroll
;     for (int i = 0; i < 16; ++i) p0[i] = __builtin_amdgcn_exp2f(p0[i]);
; #pragma unroll
;     for (int i = 0; i < 16; ++i) p1[i] = __builtin_amdgcn_exp2f(p1[i]);
;     return alpha;
; }
; DI bf16x8 at_pack(const f32x16& p, int s8) {
;     u32x4 w; w.x = at_cvtpk(p[s8], p[s8 + 1]); w.y = at_cvtpk(p[s8 + 2], p[s8 + 3]); w.z = at_cvtpk(p[s8 + 4], p[s8 + 5]); w.w = at_cvtpk(p[s8 + 6], p[s8 + 7]);
;     return __builtin_bit_cast(bf16x8, w);
; }
; template <int D0> DI void at_pv_block(f32x16 (&o)[4], int vb, const bf16x8 (&pf)[4]) {
;     const s16x4 l0 = at_tr_read<D0 * 512 + 0 * 4096>(vb), h0 = at_tr_read<D0 * 512 + 0 * 4096 + 2048>(vb), l1 = at_tr_read<D0 * 512 + 1 * 4096>(vb), h1 = at_tr_read<D0 * 512 + 1 * 4096 + 2048>(vb);
;     const s16x4 l2 = at_tr_read<D0 * 512 + 2 * 4096>(vb), h2 = at_tr_read<D0 * 512 + 2 * 4096 + 2048>(vb), l3 = at_tr_read<D0 * 512 + 3 * 4096>(vb), h3 = at_tr_read<D0 * 512 + 3 * 4096 + 2048>(vb);
;     asm volatile("s_waitcnt lgkmcnt(0)" ::: "memory"); __builtin_amdgcn_sched_barrier(0);
;     ...
;     o[D0] = MFMA32(AT_PK(l0, h0), pf[0], o[D0]); o[D0] = MFMA32(AT_PK(l1, h1), pf[1], o[D0]); o[D0] = MFMA32(AT_PK(l2, h2), pf[2], o[D0]); o[D0] = MFMA32(AT_PK(l3, h3), pf[3], o[D0]);
.LBB0_801:
	v_subrev_u32_e32 v87, s57, v160
	v_add_u32_e32 v87, s49, v87
	ds_read_b64_tr_b16 v[170:171], v87 offset:0x0
	ds_read_b64_tr_b16 v[172:173], v87 offset:0x800
	ds_read_b64_tr_b16 v[174:175], v87 offset:0x200
	ds_read_b64_tr_b16 v[176:177], v87 offset:0xa00
	ds_read_b64_tr_b16 v[178:179], v87 offset:0x400
	ds_read_b64_tr_b16 v[180:181], v87 offset:0xc00
	ds_read_b64_tr_b16 v[182:183], v87 offset:0x600
	ds_read_b64_tr_b16 v[184:185], v87 offset:0xe00
	v_exp_f32_e32 v112, v112
	v_exp_f32_e32 v113, v113
	v_exp_f32_e32 v114, v114
	v_exp_f32_e32 v115, v115
	v_exp_f32_e32 v116, v116
	v_exp_f32_e32 v117, v117
	v_exp_f32_e32 v118, v118
	v_exp_f32_e32 v119, v119
	v_cvt_pk_bf16_f32 v2, v112, v113
	v_cvt_pk_bf16_f32 v3, v114, v115
	v_cvt_pk_bf16_f32 v4, v116, v117
	v_cvt_pk_bf16_f32 v5, v118, v119
	s_waitcnt lgkmcnt(0)
	ds_read_b64_tr_b16 v[186:187], v87 offset:0x1000
	ds_read_b64_tr_b16 v[188:189], v87 offset:0x1800
	ds_read_b64_tr_b16 v[190:191], v87 offset:0x1200
	ds_read_b64_tr_b16 v[192:193], v87 offset:0x1a00
	ds_read_b64_tr_b16 v[88:89], v87 offset:0x1400
	ds_read_b64_tr_b16 v[90:91], v87 offset:0x1c00
	ds_read_b64_tr_b16 v[92:93], v87 offset:0x1600
	ds_read_b64_tr_b16 v[94:95], v87 offset:0x1e00
	v_mfma_f32_32x32x16_bf16 v[64:79], v[170:173], v[2:5], v[64:79]
	v_exp_f32_e32 v120, v120
	v_exp_f32_e32 v121, v121
	v_add_f32_e32 v81, v112, v113
	v_add_f32_e32 v82, v114, v115
	v_mfma_f32_32x32x16_bf16 v[48:63], v[174:177], v[2:5], v[48:63]
	v_exp_f32_e32 v122, v122
	v_exp_f32_e32 v123, v123
	v_cvt_pk_bf16_f32 v6, v120, v121
	v_add_f32_e32 v83, v116, v117
	v_add_f32_e32 v84, v118, v119
	v_mfma_f32_32x32x16_bf16 v[32:47], v[178:181], v[2:5], v[32:47]
	v_exp_f32_e32 v124, v124
	v_exp_f32_e32 v125, v125
	v_cvt_pk_bf16_f32 v7, v122, v123
	v_add_f32_e32 v81, v81, v82
	v_add_f32_e32 v83, v83, v84
	v_mfma_f32_32x32x16_bf16 v[16:31], v[182:185], v[2:5], v[16:31]
	v_exp_f32_e32 v126, v126
	v_exp_f32_e32 v127, v127
	v_cvt_pk_bf16_f32 v8, v124, v125
	v_add_f32_e32 v81, v81, v83
	v_add_f32_e32 v80, v80, v81
	v_cvt_pk_bf16_f32 v9, v126, v127
	s_waitcnt lgkmcnt(0)
	ds_read_b64_tr_b16 v[170:171], v87 offset:0x2000
	ds_read_b64_tr_b16 v[172:173], v87 offset:0x2800
	ds_read_b64_tr_b16 v[174:175], v87 offset:0x2200
	ds_read_b64_tr_b16 v[176:177], v87 offset:0x2a00
	ds_read_b64_tr_b16 v[178:179], v87 offset:0x2400
	ds_read_b64_tr_b16 v[180:181], v87 offset:0x2c00
	ds_read_b64_tr_b16 v[182:183], v87 offset:0x2600
	ds_read_b64_tr_b16 v[184:185], v87 offset:0x2e00
	v_mfma_f32_32x32x16_bf16 v[64:79], v[186:189], v[6:9], v[64:79]
	v_exp_f32_e32 v96, v96
	v_exp_f32_e32 v97, v97
	v_add_f32_e32 v81, v120, v121
	v_add_f32_e32 v82, v122, v123
	v_mfma_f32_32x32x16_bf16 v[48:63], v[190:193], v[6:9], v[48:63]
	v_exp_f32_e32 v98, v98
	v_exp_f32_e32 v99, v99
	v_cvt_pk_bf16_f32 v10, v96, v97
	v_add_f32_e32 v83, v124, v125
	v_add_f32_e32 v84, v126, v127
	v_mfma_f32_32x32x16_bf16 v[32:47], v[88:91], v[6:9], v[32:47]
	v_exp_f32_e32 v100, v100
	v_exp_f32_e32 v101, v101
	v_cvt_pk_bf16_f32 v11, v98, v99
	v_add_f32_e32 v81, v81, v82
	v_add_f32_e32 v83, v83, v84
	v_mfma_f32_32x32x16_bf16 v[16:31], v[92:95], v[6:9], v[16:31]
	v_exp_f32_e32 v102, v102
	v_exp_f32_e32 v103, v103
	v_cvt_pk_bf16_f32 v12, v100, v101
	v_add_f32_e32 v81, v81, v83
	v_add_f32_e32 v80, v80, v81
	v_cvt_pk_bf16_f32 v13, v102, v103
	s_waitcnt lgkmcnt(0)
	ds_read_b64_tr_b16 v[186:187], v87 offset:0x3000
	ds_read_b64_tr_b16 v[188:189], v87 offset:0x3800
	ds_read_b64_tr_b16 v[190:191], v87 offset:0x3200
	ds_read_b64_tr_b16 v[192:193], v87 offset:0x3a00
	ds_read_b64_tr_b16 v[88:89], v87 offset:0x3400
	ds_read_b64_tr_b16 v[90:91], v87 offset:0x3c00
	ds_read_b64_tr_b16 v[92:93], v87 offset:0x3600
	ds_read_b64_tr_b16 v[94:95], v87 offset:0x3e00
	v_mfma_f32_32x32x16_bf16 v[64:79], v[170:173], v[10:13], v[64:79]
	v_exp_f32_e32 v104, v104
	v_exp_f32_e32 v105, v105
	v_add_f32_e32 v81, v96, v97
	v_add_f32_e32 v82, v98, v99
	v_mfma_f32_32x32x16_bf16 v[48:63], v[174:177], v[10:13], v[48:63]
	v_exp_f32_e32 v106, v106
	v_exp_f32_e32 v107, v107
	v_cvt_pk_bf16_f32 v166, v104, v105
	v_add_f32_e32 v83, v100, v101
	v_add_f32_e32 v84, v102, v103
	v_mfma_f32_32x32x16_bf16 v[32:47], v[178:181], v[10:13], v[32:47]
	v_exp_f32_e32 v108, v108
	v_exp_f32_e32 v109, v109
	v_cvt_pk_bf16_f32 v167, v106, v107
	v_add_f32_e32 v81, v81, v82
	v_add_f32_e32 v83, v83, v84
	v_mfma_f32_32x32x16_bf16 v[16:31], v[182:185], v[10:13], v[16:31]
	v_exp_f32_e32 v110, v110
	v_exp_f32_e32 v111, v111
	v_cvt_pk_bf16_f32 v168, v108, v109
	v_add_f32_e32 v81, v81, v83
	v_add_f32_e32 v80, v80, v81
	v_cvt_pk_bf16_f32 v169, v110, v111
	s_waitcnt lgkmcnt(0)
	s_nop 1
	v_mfma_f32_32x32x16_bf16 v[64:79], v[186:189], v[166:169], v[64:79]
	v_add_f32_e32 v81, v104, v105
	v_add_f32_e32 v82, v106, v107
	v_mfma_f32_32x32x16_bf16 v[48:63], v[190:193], v[166:169], v[48:63]
	v_add_f32_e32 v83, v108, v109
	v_add_f32_e32 v84, v110, v111
	v_mfma_f32_32x32x16_bf16 v[32:47], v[88:91], v[166:169], v[32:47]
	v_add_f32_e32 v81, v81, v82
	v_add_f32_e32 v83, v83, v84
	v_mfma_f32_32x32x16_bf16 v[16:31], v[92:95], v[166:169], v[16:31]
	v_add_f32_e32 v81, v81, v83
	v_add_f32_e32 v80, v80, v81
	s_mov_b64 s[38:39], 0
	s_mov_b64 s[58:59], -1
	s_and_b64 vcc, exec, s[40:41]
	s_cbranch_vccz .LBB0_790

; #define LAS __attribute__((address_space(3)))
; DI float max_x32(float v, int lane) { return fmaxf(v, bpx(v, lane, 32)); }
; #define MFMA32(a, b, c) __builtin_amdgcn_mfma_f32_32x32x16_bf16((a), (b), (c), 0, 0, 0)
; DI unsigned at_cvtpk(float lo, float hi) { unsigned r; asm volatile("v_cvt_pk_bf16_f32 %0, %1, %2" : "=v"(r) : "v"(lo), "v"(hi)); return r; }
; DI float at_softmax(f32x16& p0, f32x16& p1, float& m_run, bool first, bool nearb, LAS const float* tabp, int lane) {
;     if (nearb) {
; #pragma unroll
;         for (int i = 0; i < 16; ++i) { p0[i] += tabp[8 * (i >> 2) + (i & 3)]; p1[i] += tabp[32 + 8 * (i >> 2) + (i & 3)]; }
;     }
;     float mx = p0[0];
; #pragma unroll
;     for (int i = 1; i < 16; ++i) mx = fmaxf(mx, p0[i]);
; #pragma unroll
;     for (int i = 0; i < 16; ++i) mx = fmaxf(mx, p1[i]);
;     float alpha = 1.f;
;     if (first || !__all(mx <= AT_THR)) {
;         mx = max_x32(mx, lane);
;         const float dl = first ? mx : fmaxf(mx, 0.f);
;         alpha = first ? 1.f : __builtin_amdgcn_exp2f(-dl); m_run += dl;
; #pragma unroll
;         for (int i = 0; i < 16; ++i) { p0[i] -= dl; p1[i] -= dl; }
;     }
; #pragma unroll
;     for (int i = 0; i < 16; ++i) p0[i] = __builtin_amdgcn_exp2f(p0[i]);
; #pragma unroll
;     for (int i = 0; i < 16; ++i) p1[i] = __builtin_amdgcn_exp2f(p1[i]);
;     return alpha;
; }
; DI bf16x8 at_pack(const f32x16& p, int s8) {
;     u32x4 w; w.x = at_cvtpk(p[s8], p[s8 + 1]); w.y = at_cvtpk(p[s8 + 2], p[s8 + 3]); w.z = at_cvtpk(p[s8 + 4], p[s8 + 5]); w.w = at_cvtpk(p[s8 + 6], p[s8 + 7]);
;     return __builtin_bit_cast(bf16x8, w);
; }
; template <int D0> DI void at_pv_block(f32x16 (&o)[4], int vb, const bf16x8 (&pf)[4]) {
;     const s16x4 l0 = at_tr_read<D0 * 512 + 0 * 4096>(vb), h0 = at_tr_read<D0 * 512 + 0 * 4096 + 2048>(vb), l1 = at_tr_read<D0 * 512 + 1 * 4096>(vb), h1 = at_tr_read<D0 * 512 + 1 * 4096 + 2048>(vb);
;     const s16x4 l2 = at_tr_read<D0 * 512 + 2 * 4096>(vb), h2 = at_tr_read<D0 * 512 + 2 * 4096 + 2048>(vb), l3 = at_tr_read<D0 * 512 + 3 * 4096>(vb), h3 = at_tr_read<D0 * 512 + 3 * 4096 + 2048>(vb);
;     asm volatile("s_waitcnt lgkmcnt(0)" ::: "memory"); __builtin_amdgcn_sched_barrier(0);
;     ...
;     o[D0] = MFMA32(AT_PK(l0, h0), pf[0], o[D0]); o[D0] = MFMA32(AT_PK(l1, h1), pf[1], o[D0]); o[D0] = MFMA32(AT_PK(l2, h2), pf[2], o[D0]); o[D0] = MFMA32(AT_PK(l3, h3), pf[3], o[D0]);
.LBB0_844:
	v_subrev_u32_e32 v87, s48, v160
	v_add_u32_e32 v87, s31, v87
	ds_read_b64_tr_b16 v[170:171], v87 offset:0x0
	ds_read_b64_tr_b16 v[172:173], v87 offset:0x800
	ds_read_b64_tr_b16 v[174:175], v87 offset:0x200
	ds_read_b64_tr_b16 v[176:177], v87 offset:0xa00
	ds_read_b64_tr_b16 v[178:179], v87 offset:0x400
	ds_read_b64_tr_b16 v[180:181], v87 offset:0xc00
	ds_read_b64_tr_b16 v[182:183], v87 offset:0x600
	ds_read_b64_tr_b16 v[184:185], v87 offset:0xe00
	v_exp_f32_e32 v112, v112
	v_exp_f32_e32 v113, v113
	v_exp_f32_e32 v114, v114
	v_exp_f32_e32 v115, v115
	v_exp_f32_e32 v116, v116
	v_exp_f32_e32 v117, v117
	v_exp_f32_e32 v118, v118
	v_exp_f32_e32 v119, v119
	v_cvt_pk_bf16_f32 v2, v112, v113
	v_cvt_pk_bf16_f32 v3, v114, v115
	v_cvt_pk_bf16_f32 v4, v116, v117
	v_cvt_pk_bf16_f32 v5, v118, v119
	s_waitcnt lgkmcnt(0)
	ds_read_b64_tr_b16 v[186:187], v87 offset:0x1000
	ds_read_b64_tr_b16 v[188:189], v87 offset:0x1800
	ds_read_b64_tr_b16 v[190:191], v87 offset:0x1200
	ds_read_b64_tr_b16 v[192:193], v87 offset:0x1a00
	ds_read_b64_tr_b16 v[88:89], v87 offset:0x1400
	ds_read_b64_tr_b16 v[90:91], v87 offset:0x1c00
	ds_read_b64_tr_b16 v[92:93], v87 offset:0x1600
	ds_read_b64_tr_b16 v[94:95], v87 offset:0x1e00
	v_mfma_f32_32x32x16_bf16 v[64:79], v[170:173], v[2:5], v[64:79]
	v_exp_f32_e32 v120, v120
	v_exp_f32_e32 v121, v121
	v_add_f32_e32 v81, v112, v113
	v_add_f32_e32 v82, v114, v115
	v_mfma_f32_32x32x16_bf16 v[48:63], v[174:177], v[2:5], v[48:63]
	v_exp_f32_e32 v122, v122
	v_exp_f32_e32 v123, v123
	v_cvt_pk_bf16_f32 v6, v120, v121
	v_add_f32_e32 v83, v116, v117
	v_add_f32_e32 v84, v118, v119
	v_mfma_f32_32x32x16_bf16 v[32:47], v[178:181], v[2:5], v[32:47]
	v_exp_f32_e32 v124, v124
	v_exp_f32_e32 v125, v125
	v_cvt_pk_bf16_f32 v7, v122, v123
	v_add_f32_e32 v81, v81, v82
	v_add_f32_e32 v83, v83, v84
	v_mfma_f32_32x32x16_bf16 v[16:31], v[182:185], v[2:5], v[16:31]
	v_exp_f32_e32 v126, v126
	v_exp_f32_e32 v127, v127
	v_cvt_pk_bf16_f32 v8, v124, v125
	v_add_f32_e32 v81, v81, v83
	v_add_f32_e32 v80, v80, v81
	v_cvt_pk_bf16_f32 v9, v126, v127
	s_waitcnt lgkmcnt(0)
	ds_read_b64_tr_b16 v[170:171], v87 offset:0x2000
	ds_read_b64_tr_b16 v[172:173], v87 offset:0x2800
	ds_read_b64_tr_b16 v[174:175], v87 offset:0x2200
	ds_read_b64_tr_b16 v[176:177], v87 offset:0x2a00
	ds_read_b64_tr_b16 v[178:179], v87 offset:0x2400
	ds_read_b64_tr_b16 v[180:181], v87 offset:0x2c00
	ds_read_b64_tr_b16 v[182:183], v87 offset:0x2600
	ds_read_b64_tr_b16 v[184:185], v87 offset:0x2e00
	v_mfma_f32_32x32x16_bf16 v[64:79], v[186:189], v[6:9], v[64:79]
	v_exp_f32_e32 v96, v96
	v_exp_f32_e32 v97, v97
	v_add_f32_e32 v81, v120, v121
	v_add_f32_e32 v82, v122, v123
	v_mfma_f32_32x32x16_bf16 v[48:63], v[190:193], v[6:9], v[48:63]
	v_exp_f32_e32 v98, v98
	v_exp_f32_e32 v99, v99
	v_cvt_pk_bf16_f32 v10, v96, v97
	v_add_f32_e32 v83, v124, v125
	v_add_f32_e32 v84, v126, v127
	v_mfma_f32_32x32x16_bf16 v[32:47], v[88:91], v[6:9], v[32:47]
	v_exp_f32_e32 v100, v100
	v_exp_f32_e32 v101, v101
	v_cvt_pk_bf16_f32 v11, v98, v99
	v_add_f32_e32 v81, v81, v82
	v_add_f32_e32 v83, v83, v84
	v_mfma_f32_32x32x16_bf16 v[16:31], v[92:95], v[6:9], v[16:31]
	v_exp_f32_e32 v102, v102
	v_exp_f32_e32 v103, v103
	v_cvt_pk_bf16_f32 v12, v100, v101
	v_add_f32_e32 v81, v81, v83
	v_add_f32_e32 v80, v80, v81
	v_cvt_pk_bf16_f32 v13, v102, v103
	s_waitcnt lgkmcnt(0)
	ds_read_b64_tr_b16 v[186:187], v87 offset:0x3000
	ds_read_b64_tr_b16 v[188:189], v87 offset:0x3800
	ds_read_b64_tr_b16 v[190:191], v87 offset:0x3200
	ds_read_b64_tr_b16 v[192:193], v87 offset:0x3a00
	ds_read_b64_tr_b16 v[88:89], v87 offset:0x3400
	ds_read_b64_tr_b16 v[90:91], v87 offset:0x3c00
	ds_read_b64_tr_b16 v[92:93], v87 offset:0x3600
	ds_read_b64_tr_b16 v[94:95], v87 offset:0x3e00
	v_mfma_f32_32x32x16_bf16 v[64:79], v[170:173], v[10:13], v[64:79]
	v_exp_f32_e32 v104, v104
	v_exp_f32_e32 v105, v105
	v_add_f32_e32 v81, v96, v97
	v_add_f32_e32 v82, v98, v99
	v_mfma_f32_32x32x16_bf16 v[48:63], v[174:177], v[10:13], v[48:63]
	v_exp_f32_e32 v106, v106
	v_exp_f32_e32 v107, v107
	v_cvt_pk_bf16_f32 v166, v104, v105
	v_add_f32_e32 v83, v100, v101
	v_add_f32_e32 v84, v102, v103
	v_mfma_f32_32x32x16_bf16 v[32:47], v[178:181], v[10:13], v[32:47]
	v_exp_f32_e32 v108, v108
	v_exp_f32_e32 v109, v109
	v_cvt_pk_bf16_f32 v167, v106, v107
	v_add_f32_e32 v81, v81, v82
	v_add_f32_e32 v83, v83, v84
	v_mfma_f32_32x32x16_bf16 v[16:31], v[182:185], v[10:13], v[16:31]
	v_exp_f32_e32 v110, v110
	v_exp_f32_e32 v111, v111
	v_cvt_pk_bf16_f32 v168, v108, v109
	v_add_f32_e32 v81, v81, v83
	v_add_f32_e32 v80, v80, v81
	v_cvt_pk_bf16_f32 v169, v110, v111
	s_waitcnt lgkmcnt(0)
	s_nop 1
	v_mfma_f32_32x32x16_bf16 v[64:79], v[186:189], v[166:169], v[64:79]
	v_add_f32_e32 v81, v104, v105
	v_add_f32_e32 v82, v106, v107
	v_mfma_f32_32x32x16_bf16 v[48:63], v[190:193], v[166:169], v[48:63]
	v_add_f32_e32 v83, v108, v109
	v_add_f32_e32 v84, v110, v111
	v_mfma_f32_32x32x16_bf16 v[32:47], v[88:91], v[166:169], v[32:47]
	v_add_f32_e32 v81, v81, v82
	v_add_f32_e32 v83, v83, v84
	v_mfma_f32_32x32x16_bf16 v[16:31], v[92:95], v[166:169], v[16:31]
	v_add_f32_e32 v81, v81, v83
	v_add_f32_e32 v80, v80, v81
	s_mov_b64 s[42:43], 0
	s_mov_b64 s[58:59], -1
	s_and_b64 vcc, exec, s[76:77]
	s_cbranch_vccz .LBB0_833
